# norm1 row loop without the per-row prefetch drain (re-measure after a first measure that did not complete)
# baseline (speedup 1.0000x reference)
; __device__ __forceinline__ float bflo(unsigned w) { return __uint_as_float(w << 16); }
; __device__ __forceinline__ float bfhi(unsigned w) { return __uint_as_float(w & 0xffff0000u); }
; __device__ __forceinline__ void phase_norm1(const Params& p, const Ctx& F, const int l) {
;     ...
;     for (; t < TPB; t += tstride) {
;         const bool isctx = t < CTXL;
;         const int mrow = isctx ? 8 : b;
;         const float* xs; float* xd; row_ptrs(p, F, l, b, t, xs, xd);
;         f32x4 v[8];
; #pragma unroll
;         for (int j = 0; j < 8; ++j) v[j] = vn[j] + (f32x4){bflo(dn[j].x), bfhi(dn[j].x), bflo(dn[j].y), bfhi(dn[j].y)};
;         if (comb) {
;             const float* gt = F.mod + (size_t)((l - 1) * 9 + mrow) * MODW + 5 * DM;
; #pragma unroll
;             for (int j = 0; j < 8; ++j) { v[j] += *((const f32x4*)gt + F.lane + 64 * j) * accn[j] * (1.f / Y_SCALE); if (!fin) *((f32x4*)xd + F.lane + 64 * j) = v[j]; }
;         }
.LBB0_157:
	v_readlane_b32 s14, v254, 31
	v_readlane_b32 s15, v254, 32
	s_and_b64 s[0:1], s[0:1], exec
	s_waitcnt vmcnt(0)
	v_lshlrev_b32_e32 v132, 16, v164
	v_and_b32_e32 v133, 0xffff0000, v164
	v_lshlrev_b32_e32 v134, 16, v165
	v_and_b32_e32 v135, 0xffff0000, v165
	v_lshlrev_b32_e32 v136, 16, v166
	v_and_b32_e32 v137, 0xffff0000, v166
	v_lshlrev_b32_e32 v138, 16, v167
	v_and_b32_e32 v139, 0xffff0000, v167
	v_lshlrev_b32_e32 v140, 16, v168
	v_and_b32_e32 v141, 0xffff0000, v168
	v_lshlrev_b32_e32 v142, 16, v169
	v_and_b32_e32 v143, 0xffff0000, v169
	v_lshlrev_b32_e32 v144, 16, v170
	v_and_b32_e32 v145, 0xffff0000, v170
	v_lshlrev_b32_e32 v146, 16, v171
	v_and_b32_e32 v147, 0xffff0000, v171
	v_lshlrev_b32_e32 v148, 16, v172
	v_and_b32_e32 v149, 0xffff0000, v172
	v_lshlrev_b32_e32 v150, 16, v173
	v_and_b32_e32 v151, 0xffff0000, v173
	v_lshlrev_b32_e32 v152, 16, v176
	v_and_b32_e32 v153, 0xffff0000, v176
	v_lshlrev_b32_e32 v154, 16, v177
	v_and_b32_e32 v155, 0xffff0000, v177
	v_lshlrev_b32_e32 v156, 16, v178
	v_and_b32_e32 v157, 0xffff0000, v178
	v_lshlrev_b32_e32 v158, 16, v179
	v_and_b32_e32 v159, 0xffff0000, v179
	v_lshlrev_b32_e32 v160, 16, v174
	v_and_b32_e32 v161, 0xffff0000, v174
	v_lshlrev_b32_e32 v162, 16, v175
	v_and_b32_e32 v163, 0xffff0000, v175
	v_cndmask_b32_e64 v1, 0, 1, s[14:15]
	s_cselect_b32 s30, 8, s19
	v_pk_add_f32 v[134:135], v[38:39], v[134:135]
	v_pk_add_f32 v[132:133], v[36:37], v[132:133]
	v_pk_add_f32 v[138:139], v[42:43], v[138:139]
	v_pk_add_f32 v[136:137], v[40:41], v[136:137]
	v_pk_add_f32 v[142:143], v[46:47], v[142:143]
	v_pk_add_f32 v[140:141], v[44:45], v[140:141]
	v_pk_add_f32 v[146:147], v[50:51], v[146:147]
	v_pk_add_f32 v[144:145], v[48:49], v[144:145]
	v_pk_add_f32 v[150:151], v[54:55], v[150:151]
	v_pk_add_f32 v[148:149], v[52:53], v[148:149]
	v_pk_add_f32 v[154:155], v[58:59], v[154:155]
	v_pk_add_f32 v[152:153], v[56:57], v[152:153]
	v_pk_add_f32 v[158:159], v[62:63], v[158:159]
	v_pk_add_f32 v[156:157], v[60:61], v[156:157]
	v_pk_add_f32 v[162:163], v[66:67], v[162:163]
	v_cmp_ne_u32_e64 s[0:1], 1, v1
	s_andn2_b64 vcc, exec, s[14:15]
	v_pk_add_f32 v[160:161], v[64:65], v[160:161]
	s_cbranch_vccnz .LBB0_159
	s_lshl_b64 s[2:3], s[2:3], 13
	s_add_u32 s2, s12, s2
	s_addc_u32 s3, s13, s3
	s_add_i32 s12, s23, s30
	s_mul_hi_u32 s13, s12, 0xc000
	s_mul_i32 s12, s12, 0xc000
	s_add_u32 s12, s24, s12
	s_addc_u32 s13, s25, s13
	v_lshl_add_u64 v[198:199], s[12:13], 0, v[34:35]
	s_mov_b32 s12, 0xb000
	v_add_co_u32_e32 v200, vcc, s12, v198
	s_mov_b64 s[12:13], 0xa000
	s_nop 0
	v_addc_co_u32_e32 v201, vcc, 0, v199, vcc
	v_lshl_add_u64 v[198:199], v[198:199], 0, s[12:13]
	global_load_dwordx4 v[210:213], v[200:201], off offset:-4096
	global_load_dwordx4 v[224:227], v[198:199], off offset:1024
	global_load_dwordx4 v[228:231], v[198:199], off offset:2048
	global_load_dwordx4 v[232:235], v[198:199], off offset:3072
	global_load_dwordx4 v[236:239], v[200:201], off
	global_load_dwordx4 v[240:243], v[200:201], off offset:1024
	global_load_dwordx4 v[244:247], v[200:201], off offset:2048
	global_load_dwordx4 v[248:251], v[200:201], off offset:3072
	s_mov_b32 s12, 0x3d000000
	s_waitcnt vmcnt(0)
	v_pk_mul_f32 v[212:213], v[4:5], v[212:213]
	v_pk_mul_f32 v[210:211], v[2:3], v[210:211]
	v_pk_fma_f32 v[134:135], v[212:213], s[12:13], v[134:135] op_sel_hi:[1,0,1]
	v_pk_fma_f32 v[132:133], v[210:211], s[12:13], v[132:133] op_sel_hi:[1,0,1]
	global_store_dwordx4 v34, v[132:135], s[2:3]
	v_pk_mul_f32 v[226:227], v[8:9], v[226:227]
	v_pk_mul_f32 v[224:225], v[6:7], v[224:225]
	v_pk_fma_f32 v[138:139], v[226:227], s[12:13], v[138:139] op_sel_hi:[1,0,1]
	v_pk_fma_f32 v[136:137], v[224:225], s[12:13], v[136:137] op_sel_hi:[1,0,1]
	global_store_dwordx4 v34, v[136:139], s[2:3] offset:1024
	v_pk_mul_f32 v[230:231], v[12:13], v[230:231]
	v_pk_mul_f32 v[228:229], v[10:11], v[228:229]
	v_pk_fma_f32 v[142:143], v[230:231], s[12:13], v[142:143] op_sel_hi:[1,0,1]
	v_pk_fma_f32 v[140:141], v[228:229], s[12:13], v[140:141] op_sel_hi:[1,0,1]
	global_store_dwordx4 v34, v[140:143], s[2:3] offset:2048
	v_pk_mul_f32 v[234:235], v[16:17], v[234:235]
	v_pk_mul_f32 v[232:233], v[14:15], v[232:233]
	v_pk_fma_f32 v[146:147], v[234:235], s[12:13], v[146:147] op_sel_hi:[1,0,1]
	v_pk_fma_f32 v[144:145], v[232:233], s[12:13], v[144:145] op_sel_hi:[1,0,1]
	global_store_dwordx4 v34, v[144:147], s[2:3] offset:3072
	v_lshl_add_u64 v[198:199], s[2:3], 0, v[34:35]
	v_add_co_u32_e32 v198, vcc, 0x1000, v198
	s_nop 1
	v_addc_co_u32_e32 v199, vcc, 0, v199, vcc
	v_pk_mul_f32 v[238:239], v[20:21], v[238:239]
	v_pk_mul_f32 v[236:237], v[18:19], v[236:237]
	v_pk_fma_f32 v[150:151], v[238:239], s[12:13], v[150:151] op_sel_hi:[1,0,1]
	v_pk_fma_f32 v[148:149], v[236:237], s[12:13], v[148:149] op_sel_hi:[1,0,1]
	global_store_dwordx4 v[198:199], v[148:151], off
	v_pk_mul_f32 v[242:243], v[24:25], v[242:243]
	v_pk_mul_f32 v[240:241], v[22:23], v[240:241]
	v_pk_fma_f32 v[154:155], v[242:243], s[12:13], v[154:155] op_sel_hi:[1,0,1]
	v_pk_fma_f32 v[152:153], v[240:241], s[12:13], v[152:153] op_sel_hi:[1,0,1]
	global_store_dwordx4 v[198:199], v[152:155], off offset:1024
	v_pk_mul_f32 v[246:247], v[28:29], v[246:247]
	v_pk_mul_f32 v[244:245], v[26:27], v[244:245]
	v_pk_fma_f32 v[158:159], v[246:247], s[12:13], v[158:159] op_sel_hi:[1,0,1]
	v_pk_fma_f32 v[156:157], v[244:245], s[12:13], v[156:157] op_sel_hi:[1,0,1]
	global_store_dwordx4 v[198:199], v[156:159], off offset:2048
	v_pk_mul_f32 v[250:251], v[32:33], v[250:251]
	v_pk_mul_f32 v[248:249], v[30:31], v[248:249]
	v_pk_fma_f32 v[162:163], v[250:251], s[12:13], v[162:163] op_sel_hi:[1,0,1]
	v_pk_fma_f32 v[160:161], v[248:249], s[12:13], v[160:161] op_sel_hi:[1,0,1]
	global_store_dwordx4 v[198:199], v[160:163], off offset:3072

; __device__ __forceinline__ void phase_norm1(const Params& p, const Ctx& F, const int l) {
;     ...
;         if (mrow != cur_m) { cur_m = mrow;
;             if (!fin) {
;                 const float* mr = F.mod + (size_t)(l * 9 + mrow) * MODW;
; #pragma unroll
;                 for (int j = 0; j < 8; ++j) { const f32x4 g = *((const f32x4*)(p.g_mix + l * DM) + F.lane + 64 * j), sc = *((const f32x4*)(mr + DM) + F.lane + 64 * j);
;                     A[j] = g * (sc + 1.f); Bv[j] = *((const f32x4*)mr + F.lane + 64 * j); }
;             }
;         }
;         float ss = 0.f;
; #pragma unroll
;         for (int j = 0; j < 8; ++j) ss += (v[j].x * v[j].x + v[j].y * v[j].y) + (v[j].z * v[j].z + v[j].w * v[j].w);
;         const float rstd = rsqrtf(wave_sum(ss) * (1.f / DM) + EPS);
.LBB0_172:
	s_cmp_eq_u32 s30, s34
	s_cbranch_scc1 .LBB0_174
	s_add_i32 s0, s30, s22
	s_mul_i32 s60, s0, 0x3000
	s_lshl_b64 s[0:1], s[60:61], 2
	s_add_u32 s0, s24, s0
	s_addc_u32 s1, s25, s1
	v_lshl_add_u64 v[108:109], s[0:1], 0, v[34:35]
	s_mov_b64 s[12:13], 0x2000
	v_lshl_add_u64 v[96:97], v[108:109], 0, s[12:13]
	s_movk_i32 s12, 0x3000
	v_add_co_u32_e32 v124, vcc, s12, v108
	global_load_dwordx4 v[68:71], v[186:187], off
	s_nop 0
	v_addc_co_u32_e32 v125, vcc, 0, v109, vcc
	global_load_dwordx4 v[72:75], v[124:125], off offset:-4096
	s_waitcnt vmcnt(0)
	v_pk_add_f32 v[74:75], v[74:75], 1.0 op_sel_hi:[1,0]
	v_pk_add_f32 v[72:73], v[72:73], 1.0 op_sel_hi:[1,0]
	v_pk_mul_f32 v[70:71], v[70:71], v[74:75]
	v_pk_mul_f32 v[68:69], v[68:69], v[72:73]
	global_load_dwordx4 v[72:75], v34, s[0:1]
	global_load_dwordx4 v[76:79], v[186:187], off offset:1024
	global_load_dwordx4 v[80:83], v[96:97], off offset:1024
	s_waitcnt vmcnt(0)
	v_pk_add_f32 v[82:83], v[82:83], 1.0 op_sel_hi:[1,0]
	v_pk_add_f32 v[80:81], v[80:81], 1.0 op_sel_hi:[1,0]
	v_pk_mul_f32 v[78:79], v[78:79], v[82:83]
	v_pk_mul_f32 v[76:77], v[76:77], v[80:81]
	global_load_dwordx4 v[80:83], v34, s[0:1] offset:1024
	global_load_dwordx4 v[84:87], v[186:187], off offset:2048
	global_load_dwordx4 v[88:91], v[96:97], off offset:2048
	s_waitcnt vmcnt(0)
	v_pk_add_f32 v[90:91], v[90:91], 1.0 op_sel_hi:[1,0]
	v_pk_add_f32 v[88:89], v[88:89], 1.0 op_sel_hi:[1,0]
	v_pk_mul_f32 v[86:87], v[86:87], v[90:91]
	v_pk_mul_f32 v[84:85], v[84:85], v[88:89]
	global_load_dwordx4 v[88:91], v34, s[0:1] offset:2048
	global_load_dwordx4 v[92:95], v[186:187], off offset:3072
	s_nop 0
	global_load_dwordx4 v[96:99], v[96:97], off offset:3072
	s_waitcnt vmcnt(0)
	v_pk_add_f32 v[98:99], v[98:99], 1.0 op_sel_hi:[1,0]
	v_pk_add_f32 v[96:97], v[96:97], 1.0 op_sel_hi:[1,0]
	v_pk_mul_f32 v[94:95], v[94:95], v[98:99]
	v_pk_mul_f32 v[92:93], v[92:93], v[96:97]
	global_load_dwordx4 v[96:99], v34, s[0:1] offset:3072
	global_load_dwordx4 v[100:103], v[188:189], off
	global_load_dwordx4 v[104:107], v[124:125], off
	s_movk_i32 s0, 0x1000
	v_add_co_u32_e32 v198, vcc, s0, v108
	s_waitcnt vmcnt(0)
	v_pk_add_f32 v[106:107], v[106:107], 1.0 op_sel_hi:[1,0]
	v_pk_add_f32 v[104:105], v[104:105], 1.0 op_sel_hi:[1,0]
	v_addc_co_u32_e32 v199, vcc, 0, v109, vcc
	v_pk_mul_f32 v[102:103], v[102:103], v[106:107]
	v_pk_mul_f32 v[100:101], v[100:101], v[104:105]
	global_load_dwordx4 v[104:107], v[198:199], off
	global_load_dwordx4 v[108:111], v[190:191], off
	global_load_dwordx4 v[112:115], v[124:125], off offset:1024
	s_waitcnt vmcnt(0)
	v_pk_add_f32 v[114:115], v[114:115], 1.0 op_sel_hi:[1,0]
	v_pk_add_f32 v[112:113], v[112:113], 1.0 op_sel_hi:[1,0]
	v_pk_mul_f32 v[110:111], v[110:111], v[114:115]
	v_pk_mul_f32 v[108:109], v[108:109], v[112:113]
	global_load_dwordx4 v[112:115], v[198:199], off offset:1024
	global_load_dwordx4 v[116:119], v[192:193], off
	global_load_dwordx4 v[120:123], v[124:125], off offset:2048
	s_waitcnt vmcnt(0)
	v_pk_add_f32 v[122:123], v[122:123], 1.0 op_sel_hi:[1,0]
	v_pk_add_f32 v[120:121], v[120:121], 1.0 op_sel_hi:[1,0]
	v_pk_mul_f32 v[118:119], v[118:119], v[122:123]
	v_pk_mul_f32 v[116:117], v[116:117], v[120:121]
	global_load_dwordx4 v[120:123], v[198:199], off offset:2048
	global_load_dwordx4 v[128:131], v[194:195], off
	s_nop 0
	global_load_dwordx4 v[124:127], v[124:125], off offset:3072
	s_waitcnt vmcnt(0)
	v_pk_add_f32 v[126:127], v[126:127], 1.0 op_sel_hi:[1,0]
	v_pk_add_f32 v[124:125], v[124:125], 1.0 op_sel_hi:[1,0]
	v_pk_mul_f32 v[126:127], v[130:131], v[126:127]
	v_pk_mul_f32 v[124:125], v[128:129], v[124:125]
	global_load_dwordx4 v[128:131], v[198:199], off offset:3072
	s_waitcnt vmcnt(0)
.LBB0_174:
	v_mov_b32_e32 v200, v137
	v_mov_b32_e32 v201, v133
	v_mov_b32_e32 v198, v136
	v_mov_b32_e32 v199, v132
	v_pk_mul_f32 v[200:201], v[200:201], v[200:201]
	v_mov_b32_e32 v210, v139
	v_mov_b32_e32 v211, v135
	v_pk_fma_f32 v[198:199], v[198:199], v[198:199], v[200:201]
	v_mov_b32_e32 v200, v138
	v_mov_b32_e32 v201, v134
	v_pk_mul_f32 v[210:211], v[210:211], v[210:211]
	s_mov_b32 s12, 0x42fe0000
	v_pk_fma_f32 v[200:201], v[200:201], v[200:201], v[210:211]
	v_pk_mul_f32 v[210:211], v[140:141], v[140:141]
	v_pk_add_f32 v[198:199], v[198:199], v[200:201]
	v_pk_mul_f32 v[200:201], v[142:143], v[142:143]
	v_pk_add_f32 v[198:199], v[198:199], v[198:199] op_sel_hi:[0,1]
	v_pk_mov_b32 v[212:213], v[210:211], v[200:201] op_sel:[1,0]
	v_mov_b32_e32 v211, v201
	v_mul_f32_e32 v198, v144, v144
	v_pk_add_f32 v[200:201], v[212:213], v[210:211]
	v_pk_fma_f32 v[210:211], v[144:145], v[144:145], v[198:199] op_sel_hi:[1,1,0]
	v_mul_f32_e32 v198, v146, v146
	v_pk_add_f32 v[200:201], v[200:201], v[200:201] op_sel_hi:[0,1]
	v_pk_fma_f32 v[212:213], v[146:147], v[146:147], v[198:199] op_sel_hi:[1,1,0]
	v_mul_f32_e32 v210, v148, v148
	v_mul_f32_e32 v212, v149, v149
	v_mul_f32_e32 v200, v150, v150
	v_mul_f32_e32 v198, v151, v151
	v_pk_add_f32 v[210:211], v[210:211], v[212:213]
	v_pk_add_f32 v[198:199], v[200:201], v[198:199]
	v_pk_mul_f32 v[200:201], v[154:155], v[154:155]
	v_pk_add_f32 v[198:199], v[210:211], v[198:199]
	v_pk_mul_f32 v[210:211], v[152:153], v[152:153]
	v_pk_add_f32 v[198:199], v[198:199], v[198:199] op_sel_hi:[0,1]
	v_pk_mov_b32 v[212:213], v[210:211], v[200:201] op_sel:[1,0]
	v_mov_b32_e32 v211, v201
	v_mul_f32_e32 v198, v156, v156
	v_pk_add_f32 v[200:201], v[212:213], v[210:211]
	v_pk_fma_f32 v[210:211], v[156:157], v[156:157], v[198:199] op_sel_hi:[1,1,0]
	v_mul_f32_e32 v198, v158, v158
	v_pk_add_f32 v[200:201], v[200:201], v[200:201] op_sel_hi:[0,1]
	v_pk_fma_f32 v[212:213], v[158:159], v[158:159], v[198:199] op_sel_hi:[1,1,0]
	v_mul_f32_e32 v210, v160, v160
	v_mul_f32_e32 v212, v161, v161
	v_mul_f32_e32 v200, v162, v162
	v_mul_f32_e32 v198, v163, v163
	v_pk_add_f32 v[210:211], v[210:211], v[212:213]
	v_pk_add_f32 v[198:199], v[200:201], v[198:199]
	s_nop 0
	v_pk_add_f32 v[198:199], v[210:211], v[198:199]
	s_nop 0
	v_add_f32_e32 v1, v198, v199
	ds_bpermute_b32 v198, v203, v1
	s_waitcnt lgkmcnt(0)
; __device__ __forceinline__ float amax4(const f32x4& v) { return fmaxf(fmaxf(fabsf(v.x), fabsf(v.y)), fmaxf(fabsf(v.z), fabsf(v.w))); }
; __device__ __forceinline__ void phase_norm1(const Params& p, const Ctx& F, const int l) {
;     ...
;         float ss = 0.f;
; #pragma unroll
;         for (int j = 0; j < 8; ++j) ss += (v[j].x * v[j].x + v[j].y * v[j].y) + (v[j].z * v[j].z + v[j].w * v[j].w);
;         const float rstd = rsqrtf(wave_sum(ss) * (1.f / DM) + EPS);
;         if (fin) {
; #pragma unroll
;             for (int j = 0; j < 8; ++j) __builtin_nontemporal_store(v[j] * rstd * *((const f32x4*)p.g_final + F.lane + 64 * j), (f32x4*)xd + F.lane + 64 * j);
;         } else {
;             float am = 0.f;
; #pragma unroll
;             for (int j = 0; j < 8; ++j) { v[j] = v[j] * rstd * A[j] + Bv[j]; am = fmaxf(am, amax4(v[j])); }
;             am = fmaxf(wave_max(am), 1e-20f); const float inv = 127.f / am;
	v_add_f32_e32 v1, v1, v198
	ds_bpermute_b32 v198, v204, v1
	s_waitcnt lgkmcnt(0)
	v_add_f32_e32 v1, v1, v198
	ds_bpermute_b32 v198, v205, v1
	s_waitcnt lgkmcnt(0)
	v_add_f32_e32 v1, v1, v198
	ds_bpermute_b32 v198, v206, v1
	s_waitcnt lgkmcnt(0)
	v_add_f32_e32 v1, v1, v198
	ds_bpermute_b32 v198, v207, v1
	s_waitcnt lgkmcnt(0)
	v_add_f32_e32 v1, v1, v198
	ds_bpermute_b32 v198, v208, v1
	s_waitcnt lgkmcnt(0)
	v_add_f32_e32 v1, v1, v198
	v_fmamk_f32 v1, v1, 0x3a000000, v196
	v_mul_f32_e32 v198, 0x4b800000, v1
	v_cmp_gt_f32_e32 vcc, s52, v1
	s_nop 1
	v_cndmask_b32_e32 v1, v1, v198, vcc
	v_rsq_f32_e32 v1, v1
	s_nop 0
	v_mul_f32_e32 v198, 0x45800000, v1
	v_cndmask_b32_e32 v198, v1, v198, vcc
	v_pk_mul_f32 v[134:135], v[134:135], v[198:199] op_sel_hi:[1,0]
	v_pk_mul_f32 v[132:133], v[132:133], v[198:199] op_sel_hi:[1,0]
	v_pk_fma_f32 v[200:201], v[70:71], v[134:135], v[74:75]
	v_pk_mul_f32 v[134:135], v[138:139], v[198:199] op_sel_hi:[1,0]
	v_pk_fma_f32 v[210:211], v[68:69], v[132:133], v[72:73]
	v_pk_mul_f32 v[132:133], v[136:137], v[198:199] op_sel_hi:[1,0]
	v_pk_fma_f32 v[136:137], v[78:79], v[134:135], v[82:83]
	v_max_f32_e64 v1, |v200|, |v201|
	v_pk_fma_f32 v[138:139], v[76:77], v[132:133], v[80:81]
	v_max_f32_e64 v132, |v136|, |v137|
	v_max3_f32 v1, |v210|, |v211|, v1
	v_max3_f32 v132, |v138|, |v139|, v132
	v_pk_mul_f32 v[134:135], v[142:143], v[198:199] op_sel_hi:[1,0]
	v_max3_f32 v1, v1, 0, v132
	v_pk_mul_f32 v[132:133], v[140:141], v[198:199] op_sel_hi:[1,0]
	v_pk_fma_f32 v[140:141], v[86:87], v[134:135], v[90:91]
	v_pk_fma_f32 v[142:143], v[84:85], v[132:133], v[88:89]
	v_max_f32_e64 v132, |v140|, |v141|
	v_max3_f32 v199, |v142|, |v143|, v132
	v_pk_mul_f32 v[134:135], v[146:147], v[198:199] op_sel_hi:[1,0]
	v_pk_mul_f32 v[132:133], v[144:145], v[198:199] op_sel_hi:[1,0]
	v_pk_fma_f32 v[144:145], v[94:95], v[134:135], v[98:99]
	v_pk_fma_f32 v[146:147], v[92:93], v[132:133], v[96:97]
	v_max_f32_e64 v132, |v144|, |v145|
	v_max3_f32 v132, |v146|, |v147|, v132
	v_pk_mul_f32 v[134:135], v[150:151], v[198:199] op_sel_hi:[1,0]
	v_max3_f32 v1, v1, v199, v132
	v_pk_mul_f32 v[132:133], v[148:149], v[198:199] op_sel_hi:[1,0]
	v_pk_fma_f32 v[148:149], v[102:103], v[134:135], v[106:107]
	v_pk_fma_f32 v[150:151], v[100:101], v[132:133], v[104:105]
	v_max_f32_e64 v132, |v148|, |v149|
	v_max3_f32 v199, |v150|, |v151|, v132
	v_pk_mul_f32 v[134:135], v[154:155], v[198:199] op_sel_hi:[1,0]
	v_pk_mul_f32 v[132:133], v[152:153], v[198:199] op_sel_hi:[1,0]
	v_pk_fma_f32 v[152:153], v[110:111], v[134:135], v[114:115]
	v_pk_fma_f32 v[154:155], v[108:109], v[132:133], v[112:113]
	v_max_f32_e64 v132, |v152|, |v153|
	v_max3_f32 v132, |v154|, |v155|, v132
	v_pk_mul_f32 v[134:135], v[158:159], v[198:199] op_sel_hi:[1,0]
	v_max3_f32 v1, v1, v199, v132
	v_pk_mul_f32 v[132:133], v[156:157], v[198:199] op_sel_hi:[1,0]
	v_pk_fma_f32 v[156:157], v[118:119], v[134:135], v[122:123]
	v_pk_fma_f32 v[158:159], v[116:117], v[132:133], v[120:121]
	v_max_f32_e64 v132, |v156|, |v157|
	v_max3_f32 v199, |v158|, |v159|, v132
	v_pk_mul_f32 v[132:133], v[162:163], v[198:199] op_sel_hi:[1,0]
	v_pk_mul_f32 v[134:135], v[160:161], v[198:199] op_sel_hi:[1,0]
	v_pk_fma_f32 v[132:133], v[126:127], v[132:133], v[130:131]
	v_pk_fma_f32 v[160:161], v[124:125], v[134:135], v[128:129]
	v_max_f32_e64 v134, |v132|, |v133|
	v_max3_f32 v134, |v160|, |v161|, v134
	v_max3_f32 v1, v1, v199, v134
	ds_bpermute_b32 v134, v203, v1
	s_waitcnt lgkmcnt(0)
	v_max_f32_e32 v134, v134, v134
	v_max_f32_e32 v1, v1, v134
	ds_bpermute_b32 v134, v204, v1
	s_waitcnt lgkmcnt(0)
	v_max_f32_e32 v134, v134, v134
	v_max_f32_e32 v1, v1, v134
	ds_bpermute_b32 v134, v205, v1
	s_waitcnt lgkmcnt(0)
	v_max_f32_e32 v134, v134, v134
	v_max_f32_e32 v1, v1, v134
	ds_bpermute_b32 v134, v206, v1
	s_waitcnt lgkmcnt(0)
	v_max_f32_e32 v134, v134, v134
	v_max_f32_e32 v1, v1, v134
	ds_bpermute_b32 v134, v207, v1
	s_waitcnt lgkmcnt(0)
	v_max_f32_e32 v134, v134, v134
	v_max_f32_e32 v1, v1, v134
	ds_bpermute_b32 v134, v208, v1
	s_waitcnt lgkmcnt(0)
; __device__ __forceinline__ unsigned pack_i8x4(float a, float b, float c, float d, float inv) { return q8u(a, inv) | (q8u(b, inv) << 8) | (q8u(c, inv) << 16) | (q8u(d, inv) << 24); }
; __device__ __forceinline__ float amax4(const f32x4& v) { return fmaxf(fmaxf(fabsf(v.x), fabsf(v.y)), fmaxf(fabsf(v.z), fabsf(v.w))); }
; __device__ __forceinline__ void phase_norm1(const Params& p, const Ctx& F, const int l) {
;     ...
;             float am = 0.f;
; #pragma unroll
;             for (int j = 0; j < 8; ++j) { v[j] = v[j] * rstd * A[j] + Bv[j]; am = fmaxf(am, amax4(v[j])); }
;             am = fmaxf(wave_max(am), 1e-20f); const float inv = 127.f / am;
;             unsigned* xn = (unsigned*)((signed char*)F.r1 + ((size_t)b * TPB + t) * DM) + F.lane;
; #pragma unroll
;             for (int j = 0; j < 8; ++j) __builtin_nontemporal_store(pack_i8x4(v[j].x, v[j].y, v[j].z, v[j].w, inv), xn + 64 * j);
;             if (F.lane == 0) F.sax[b * TPB + t] = am * (1.f / 127.f);
	v_max3_f32 v134, v1, v134, s53
	v_div_scale_f32 v1, s[0:1], v134, v134, s12
	v_rcp_f32_e32 v135, v1
	s_ashr_i32 s1, s20, 31
	s_add_u32 s0, s21, s20
	s_addc_u32 s1, 0, s1
	v_fma_f32 v162, -v1, v135, 1.0
	v_fmac_f32_e32 v135, v162, v135
	v_div_scale_f32 v162, vcc, s12, v134, s12
	v_mul_f32_e32 v163, v162, v135
	v_fma_f32 v198, -v1, v163, v162
	v_fmac_f32_e32 v163, v198, v135
	v_fma_f32 v1, -v1, v163, v162
	v_div_fmas_f32 v1, v1, v135, v163
	v_div_fixup_f32 v1, v1, v134, s12
	v_mul_f32_e32 v162, v211, v1
	v_mul_f32_e32 v199, v200, v1
	v_mul_f32_e32 v135, v210, v1
	v_rndne_f32_e32 v162, v162
	v_rndne_f32_e32 v199, v199
	v_mul_f32_e32 v200, v201, v1
	v_rndne_f32_e32 v135, v135
	v_cvt_i32_f32_e32 v198, v162
	v_cvt_i32_f32_e32 v199, v199
	v_rndne_f32_e32 v200, v200
	v_cvt_i32_f32_e32 v135, v135
	v_cvt_i32_f32_e32 v200, v200
	v_mul_f32_e32 v138, v138, v1
	v_mul_f32_e32 v137, v137, v1
	v_rndne_f32_e32 v138, v138
	v_mul_f32_e32 v139, v139, v1
	v_mul_f32_e32 v136, v136, v1
	v_rndne_f32_e32 v137, v137
	v_med3_i32 v198, v198, s80, v218
	v_med3_i32 v199, v199, s80, v218
	v_cvt_i32_f32_e32 v138, v138
	v_rndne_f32_e32 v139, v139
	v_rndne_f32_e32 v136, v136
	v_cvt_i32_f32_e32 v137, v137
	v_med3_i32 v135, v135, s80, v218
	v_lshlrev_b32_e32 v198, 8, v198
	v_lshlrev_b32_e32 v199, 16, v199
	v_med3_i32 v200, v200, s80, v218
	v_cvt_i32_f32_e32 v139, v139
	v_cvt_i32_f32_e32 v136, v136
	s_lshl_b64 s[0:1], s[0:1], 11
	v_and_b32_e32 v198, 0xff00, v198
	v_and_b32_e32 v199, 0xff0000, v199
	v_perm_b32 v135, v200, v135, s81
	v_lshl_add_u64 v[162:163], v[180:181], 0, s[0:1]
	v_or3_b32 v135, v135, v198, v199
	global_store_dword v[162:163], v135, off nt
	v_med3_i32 v135, v138, s80, v218
	v_med3_i32 v137, v137, s80, v218
	v_med3_i32 v138, v139, s80, v218
	v_med3_i32 v136, v136, s80, v218
	v_perm_b32 v135, v137, v135, s81
	v_mul_f32_e32 v137, v142, v1
	v_lshlrev_b32_e32 v138, 8, v138
	v_lshlrev_b32_e32 v136, 16, v136
	v_rndne_f32_e32 v137, v137
	v_and_b32_e32 v138, 0xff00, v138
	v_and_b32_e32 v136, 0xff0000, v136
	v_cvt_i32_f32_e32 v137, v137
	v_or3_b32 v135, v135, v138, v136
	v_mul_f32_e32 v138, v141, v1
	v_rndne_f32_e32 v138, v138
	v_cvt_i32_f32_e32 v138, v138
	v_mul_f32_e32 v139, v143, v1
	global_store_dword v[162:163], v135, off offset:256 nt
	v_med3_i32 v135, v137, s80, v218
	v_mul_f32_e32 v137, v140, v1
	v_rndne_f32_e32 v139, v139
	v_rndne_f32_e32 v137, v137
	v_cvt_i32_f32_e32 v139, v139
	v_cvt_i32_f32_e32 v137, v137
	v_med3_i32 v138, v138, s80, v218
	v_perm_b32 v135, v138, v135, s81
	v_mul_f32_e32 v138, v146, v1
	v_rndne_f32_e32 v138, v138
	v_med3_i32 v136, v139, s80, v218
	v_med3_i32 v137, v137, s80, v218
	v_cvt_i32_f32_e32 v138, v138
	v_lshlrev_b32_e32 v136, 8, v136
	v_lshlrev_b32_e32 v137, 16, v137
	v_and_b32_e32 v136, 0xff00, v136
	v_and_b32_e32 v137, 0xff0000, v137
	v_or3_b32 v135, v135, v136, v137
	global_store_dword v[162:163], v135, off offset:512 nt
	v_med3_i32 v135, v138, s80, v218
	v_mul_f32_e32 v138, v145, v1
	v_rndne_f32_e32 v138, v138
	v_cvt_i32_f32_e32 v138, v138
	v_mul_f32_e32 v139, v147, v1
	v_mul_f32_e32 v137, v144, v1
	v_rndne_f32_e32 v139, v139
	v_rndne_f32_e32 v137, v137
	v_cvt_i32_f32_e32 v139, v139
	v_cvt_i32_f32_e32 v137, v137
	v_med3_i32 v138, v138, s80, v218
	v_perm_b32 v135, v138, v135, s81
	v_mul_f32_e32 v138, v150, v1
	v_rndne_f32_e32 v138, v138
	v_med3_i32 v136, v139, s80, v218
	v_med3_i32 v137, v137, s80, v218
	v_cvt_i32_f32_e32 v138, v138
	v_lshlrev_b32_e32 v136, 8, v136
	v_lshlrev_b32_e32 v137, 16, v137
	v_and_b32_e32 v136, 0xff00, v136
	v_and_b32_e32 v137, 0xff0000, v137
	v_or3_b32 v135, v135, v136, v137
	global_store_dword v[162:163], v135, off offset:768 nt
	v_med3_i32 v135, v138, s80, v218
	v_mul_f32_e32 v138, v149, v1
	v_rndne_f32_e32 v138, v138
	v_cvt_i32_f32_e32 v138, v138
	v_mul_f32_e32 v139, v151, v1
	v_mul_f32_e32 v137, v148, v1
	v_rndne_f32_e32 v139, v139
	v_rndne_f32_e32 v137, v137
	v_cvt_i32_f32_e32 v139, v139
	v_cvt_i32_f32_e32 v137, v137
	v_med3_i32 v138, v138, s80, v218
	v_perm_b32 v135, v138, v135, s81
	v_mul_f32_e32 v138, v154, v1
	v_rndne_f32_e32 v138, v138
	v_med3_i32 v136, v139, s80, v218
	v_med3_i32 v137, v137, s80, v218
	v_cvt_i32_f32_e32 v138, v138
	v_lshlrev_b32_e32 v136, 8, v136
	v_lshlrev_b32_e32 v137, 16, v137
	v_and_b32_e32 v136, 0xff00, v136
	v_and_b32_e32 v137, 0xff0000, v137
	v_or3_b32 v135, v135, v136, v137
	global_store_dword v[162:163], v135, off offset:1024 nt
	v_med3_i32 v135, v138, s80, v218
	v_mul_f32_e32 v138, v153, v1
	v_rndne_f32_e32 v138, v138
	v_cvt_i32_f32_e32 v138, v138
	v_mul_f32_e32 v139, v155, v1
	v_mul_f32_e32 v137, v152, v1
	v_rndne_f32_e32 v139, v139
	v_rndne_f32_e32 v137, v137
	v_cvt_i32_f32_e32 v139, v139
	v_cvt_i32_f32_e32 v137, v137
	v_med3_i32 v138, v138, s80, v218
	v_perm_b32 v135, v138, v135, s81
	v_mul_f32_e32 v138, v158, v1
	v_rndne_f32_e32 v138, v138
	v_med3_i32 v136, v139, s80, v218
	v_med3_i32 v137, v137, s80, v218
	v_cvt_i32_f32_e32 v138, v138
	v_lshlrev_b32_e32 v136, 8, v136
	v_lshlrev_b32_e32 v137, 16, v137
	v_and_b32_e32 v136, 0xff00, v136
	v_and_b32_e32 v137, 0xff0000, v137
	v_or3_b32 v135, v135, v136, v137
	v_mul_f32_e32 v139, v159, v1
	global_store_dword v[162:163], v135, off offset:1280 nt
	v_med3_i32 v135, v138, s80, v218
	v_mul_f32_e32 v138, v157, v1
	v_rndne_f32_e32 v139, v139
	v_rndne_f32_e32 v138, v138
	v_cvt_i32_f32_e32 v139, v139
	v_cvt_i32_f32_e32 v138, v138
	v_mul_f32_e32 v137, v156, v1
	v_rndne_f32_e32 v137, v137
	v_cvt_i32_f32_e32 v137, v137
	v_med3_i32 v136, v139, s80, v218
	v_med3_i32 v138, v138, s80, v218
	v_mul_f32_e32 v139, v161, v1
	v_mul_f32_e32 v132, v132, v1
	v_perm_b32 v135, v138, v135, s81
	v_mul_f32_e32 v138, v160, v1
	v_rndne_f32_e32 v139, v139
	v_rndne_f32_e32 v132, v132
	v_mul_f32_e32 v1, v133, v1
	v_rndne_f32_e32 v138, v138
	v_cvt_i32_f32_e32 v139, v139
	v_cvt_i32_f32_e32 v132, v132
	v_rndne_f32_e32 v1, v1
	v_med3_i32 v137, v137, s80, v218
	v_cvt_i32_f32_e32 v138, v138
	v_cvt_i32_f32_e32 v1, v1
	v_lshlrev_b32_e32 v136, 8, v136
	v_lshlrev_b32_e32 v137, 16, v137
	v_and_b32_e32 v136, 0xff00, v136
	v_and_b32_e32 v137, 0xff0000, v137
	v_or3_b32 v135, v135, v136, v137
	v_med3_i32 v136, v139, s80, v218
	v_med3_i32 v132, v132, s80, v218
	global_store_dword v[162:163], v135, off offset:1536 nt
	v_med3_i32 v135, v138, s80, v218
	v_lshlrev_b32_e32 v136, 8, v136
	v_lshlrev_b32_e32 v132, 16, v132
	v_med3_i32 v1, v1, s80, v218
	v_and_b32_e32 v136, 0xff00, v136
	v_and_b32_e32 v132, 0xff0000, v132
	v_perm_b32 v1, v1, v135, s81
	v_or3_b32 v1, v1, v136, v132
	global_store_dword v[162:163], v1, off offset:1792 nt
	s_and_saveexec_b64 s[0:1], s[6:7]
	s_cbranch_execz .LBB0_152
	s_add_i32 s12, s20, s21
	s_ashr_i32 s13, s12, 31
	s_lshl_b64 s[12:13], s[12:13], 2
	s_add_u32 s12, s26, s12
	s_addc_u32 s13, s27, s13
	v_mul_f32_e32 v1, 0x3c010204, v134
	global_store_dword v35, v1, s[12:13]
	s_branch .LBB0_152

; __device__ __forceinline__ float bflo(unsigned w) { return __uint_as_float(w << 16); }
; __device__ __forceinline__ float bfhi(unsigned w) { return __uint_as_float(w & 0xffff0000u); }
; __device__ __forceinline__ void phase_norm1(const Params& p, const Ctx& F, const int l) {
;     ...
;         for (int j = 0; j < 8; ++j) v[j] = vn[j] + (f32x4){bflo(dn[j].x), bfhi(dn[j].x), bflo(dn[j].y), bfhi(dn[j].y)};
;         if (comb) {
;             const float* gt = F.mod + (size_t)((l - 1) * 9 + mrow) * MODW + 5 * DM;
; #pragma unroll
;             for (int j = 0; j < 8; ++j) { v[j] += *((const f32x4*)gt + F.lane + 64 * j) * accn[j] * (1.f / Y_SCALE); if (!fin) *((f32x4*)xd + F.lane + 64 * j) = v[j]; }
;         }
;         { const int t2 = t + tstride;
;           if (t2 < TPB) { const float* xs2; float* xd2; row_ptrs(p, F, l, b, t2, xs2, xd2);
; #pragma unroll
;             for (int j = 0; j < 8; ++j) vn[j] = __builtin_nontemporal_load((const f32x4*)xs2 + F.lane + 64 * j);
;             if (comb) {
; #pragma unroll
;                 for (int j = 0; j < 8; ++j) dn[j] = __builtin_nontemporal_load((const u32x2*)(F.dlt + ((size_t)b * TPB + t2) * DM + 4 * F.lane + 256 * j)); }
;             if (comb) { { if (fin) gather_y1(F, sn, accn); else gather_y(F, sn, accn); } const int t3 = t2 + tstride; sn = -1; if (t3 < TPB && F.lane < 16) sn = F.slot[(unsigned)((b * 16 + F.lane) * TPB + t3)]; } } }
;         if (mrow != cur_m) { cur_m = mrow;
;             if (!fin) {
;                 const float* mr = F.mod + (size_t)(l * 9 + mrow) * MODW;
; #pragma unroll
;                 for (int j = 0; j < 8; ++j) { const f32x4 g = *((const f32x4*)(p.g_mix + l * DM) + F.lane + 64 * j), sc = *((const f32x4*)(mr + DM) + F.lane + 64 * j);
;                     A[j] = g * (sc + 1.f); Bv[j] = *((const f32x4*)mr + F.lane + 64 * j); }
;             }
;         }
;         float ss = 0.f;
; #pragma unroll
;         for (int j = 0; j < 8; ++j) ss += (v[j].x * v[j].x + v[j].y * v[j].y) + (v[j].z * v[j].z + v[j].w * v[j].w);
;         const float rstd = rsqrtf(wave_sum(ss) * (1.f / DM) + EPS);
;         if (fin) {
; #pragma unroll
;             for (int j = 0; j < 8; ++j) __builtin_nontemporal_store(v[j] * rstd * *((const f32x4*)p.g_final + F.lane + 64 * j), (f32x4*)xd + F.lane + 64 * j);
.LBB0_1459:
	v_lshlrev_b32_e32 v96, 16, v146
	v_and_b32_e32 v97, 0xffff0000, v146
	v_lshlrev_b32_e32 v98, 16, v147
	v_and_b32_e32 v99, 0xffff0000, v147
	v_pk_add_f32 v[28:29], v[28:29], v[96:97]
	v_pk_add_f32 v[30:31], v[30:31], v[98:99]
	v_lshlrev_b32_e32 v96, 16, v144
	v_and_b32_e32 v97, 0xffff0000, v144
	v_lshlrev_b32_e32 v98, 16, v145
	v_and_b32_e32 v99, 0xffff0000, v145
	v_pk_add_f32 v[24:25], v[24:25], v[96:97]
	v_pk_add_f32 v[26:27], v[26:27], v[98:99]
	v_lshlrev_b32_e32 v96, 16, v142
	v_and_b32_e32 v97, 0xffff0000, v142
	v_lshlrev_b32_e32 v98, 16, v143
	v_and_b32_e32 v99, 0xffff0000, v143
	v_pk_add_f32 v[20:21], v[20:21], v[96:97]
	v_pk_add_f32 v[22:23], v[22:23], v[98:99]
	v_lshlrev_b32_e32 v96, 16, v140
	v_and_b32_e32 v97, 0xffff0000, v140
	v_lshlrev_b32_e32 v98, 16, v141
	v_and_b32_e32 v99, 0xffff0000, v141
	v_pk_add_f32 v[16:17], v[16:17], v[96:97]
	v_pk_add_f32 v[18:19], v[18:19], v[98:99]
	v_lshlrev_b32_e32 v96, 16, v138
	v_and_b32_e32 v97, 0xffff0000, v138
	v_lshlrev_b32_e32 v98, 16, v139
	v_and_b32_e32 v99, 0xffff0000, v139
	v_pk_add_f32 v[12:13], v[12:13], v[96:97]
	v_pk_add_f32 v[14:15], v[14:15], v[98:99]
	v_lshlrev_b32_e32 v96, 16, v136
	v_and_b32_e32 v97, 0xffff0000, v136
	v_lshlrev_b32_e32 v98, 16, v137
	v_and_b32_e32 v99, 0xffff0000, v137
	v_pk_add_f32 v[96:97], v[8:9], v[96:97]
	v_pk_add_f32 v[8:9], v[10:11], v[98:99]
	v_lshlrev_b32_e32 v10, 16, v134
	v_and_b32_e32 v11, 0xffff0000, v134
	v_lshlrev_b32_e32 v98, 16, v135
	v_and_b32_e32 v99, 0xffff0000, v135
	v_pk_add_f32 v[100:101], v[4:5], v[10:11]
	v_lshlrev_b32_e32 v4, 16, v132
	v_and_b32_e32 v5, 0xffff0000, v132
	v_pk_add_f32 v[98:99], v[6:7], v[98:99]
	v_lshlrev_b32_e32 v6, 16, v133
	v_and_b32_e32 v7, 0xffff0000, v133
	v_pk_add_f32 v[102:103], v[0:1], v[4:5]
	s_waitcnt vmcnt(5)
	v_pk_mul_f32 v[0:1], v[154:155], v[94:95]
	v_pk_add_f32 v[104:105], v[2:3], v[6:7]
	v_pk_mul_f32 v[2:3], v[148:149], v[92:93]
	v_pk_fma_f32 v[30:31], v[0:1], s[12:13], v[30:31] op_sel_hi:[1,0,1]
	v_pk_mul_f32 v[0:1], v[156:157], v[90:91]
	v_pk_fma_f32 v[28:29], v[2:3], s[12:13], v[28:29] op_sel_hi:[1,0,1]
	v_pk_mul_f32 v[2:3], v[150:151], v[88:89]
	v_pk_fma_f32 v[26:27], v[0:1], s[12:13], v[26:27] op_sel_hi:[1,0,1]
	v_pk_mul_f32 v[0:1], v[160:161], v[86:87]
	v_pk_fma_f32 v[24:25], v[2:3], s[12:13], v[24:25] op_sel_hi:[1,0,1]
	v_pk_mul_f32 v[2:3], v[152:153], v[84:85]
	v_pk_fma_f32 v[22:23], v[0:1], s[12:13], v[22:23] op_sel_hi:[1,0,1]
	s_waitcnt vmcnt(4)
	v_pk_mul_f32 v[0:1], v[164:165], v[82:83]
	v_pk_fma_f32 v[20:21], v[2:3], s[12:13], v[20:21] op_sel_hi:[1,0,1]
	v_pk_mul_f32 v[2:3], v[158:159], v[80:81]
	v_pk_fma_f32 v[18:19], v[0:1], s[12:13], v[18:19] op_sel_hi:[1,0,1]
	s_waitcnt vmcnt(3)
	v_pk_mul_f32 v[0:1], v[168:169], v[78:79]
	v_pk_fma_f32 v[16:17], v[2:3], s[12:13], v[16:17] op_sel_hi:[1,0,1]
	v_pk_mul_f32 v[2:3], v[162:163], v[76:77]
	v_pk_fma_f32 v[4:5], v[0:1], s[12:13], v[14:15] op_sel_hi:[1,0,1]
	s_waitcnt vmcnt(0)
	v_pk_mul_f32 v[14:15], v[174:175], v[64:65]
	v_pk_fma_f32 v[6:7], v[2:3], s[12:13], v[12:13] op_sel_hi:[1,0,1]
	v_pk_mul_f32 v[2:3], v[166:167], v[72:73]
	v_pk_mul_f32 v[12:13], v[178:179], v[66:67]
	v_pk_fma_f32 v[66:67], v[14:15], s[12:13], v[102:103] op_sel_hi:[1,0,1]
	v_mov_b32_e32 v14, v29
	v_mov_b32_e32 v15, v25
	v_pk_fma_f32 v[10:11], v[2:3], s[12:13], v[96:97] op_sel_hi:[1,0,1]
	v_pk_mul_f32 v[2:3], v[170:171], v[68:69]
	v_pk_fma_f32 v[64:65], v[12:13], s[12:13], v[104:105] op_sel_hi:[1,0,1]
	v_mov_b32_e32 v12, v28
	v_mov_b32_e32 v13, v24
	v_pk_mul_f32 v[14:15], v[14:15], v[14:15]
	v_mov_b32_e32 v68, v31
	v_mov_b32_e32 v69, v27
	v_pk_fma_f32 v[12:13], v[12:13], v[12:13], v[14:15]
	v_mov_b32_e32 v14, v30
	v_mov_b32_e32 v15, v26
	v_pk_mul_f32 v[68:69], v[68:69], v[68:69]
	v_pk_mul_f32 v[0:1], v[172:173], v[74:75]
	v_pk_fma_f32 v[14:15], v[14:15], v[14:15], v[68:69]
	v_pk_mul_f32 v[68:69], v[20:21], v[20:21]
	v_pk_add_f32 v[12:13], v[12:13], v[14:15]
	v_pk_mul_f32 v[14:15], v[22:23], v[22:23]
	v_pk_fma_f32 v[8:9], v[0:1], s[12:13], v[8:9] op_sel_hi:[1,0,1]
	v_pk_mul_f32 v[0:1], v[176:177], v[70:71]
	v_pk_mov_b32 v[70:71], v[68:69], v[14:15] op_sel:[1,0]
	v_mov_b32_e32 v69, v15
	v_pk_add_f32 v[14:15], v[70:71], v[68:69]
	v_mul_f32_e32 v68, v6, v6
	v_mul_f32_e32 v69, v7, v7
	v_pk_add_f32 v[12:13], v[12:13], v[12:13] op_sel:[0,1] op_sel_hi:[1,0]
	v_pk_add_f32 v[14:15], v[14:15], v[14:15] op_sel:[0,1] op_sel_hi:[1,0]
	v_mov_b32_e32 v13, v68
	v_mov_b32_e32 v15, v69
	v_pk_add_f32 v[68:69], v[12:13], v[14:15]
	global_load_dwordx4 v[12:15], v[180:181], off
	global_load_dwordx4 v[76:79], v[180:181], off offset:1024
	global_load_dwordx4 v[80:83], v[180:181], off offset:2048
	global_load_dwordx4 v[84:87], v[180:181], off offset:3072
	global_load_dwordx4 v[88:91], v[182:183], off
	global_load_dwordx4 v[92:95], v[184:185], off
	global_load_dwordx4 v[108:111], v[186:187], off
	global_load_dwordx4 v[112:115], v[188:189], off
	v_mul_f32_e32 v70, v17, v17
	v_mul_f32_e32 v72, v4, v4
	v_pk_fma_f32 v[70:71], v[16:17], v[16:17], v[70:71] op_sel_hi:[1,1,0]
	v_mul_f32_e32 v74, v5, v5
	v_mov_b32_e32 v71, v72
	v_mul_f32_e32 v72, v19, v19
	v_pk_fma_f32 v[72:73], v[18:19], v[18:19], v[72:73] op_sel_hi:[1,1,0]
	v_pk_fma_f32 v[0:1], v[0:1], s[12:13], v[98:99] op_sel_hi:[1,0,1]
	v_mov_b32_e32 v73, v74
	v_pk_add_f32 v[70:71], v[70:71], v[72:73]
	v_pk_mul_f32 v[72:73], v[10:11], v[10:11]
	v_pk_add_f32 v[68:69], v[68:69], v[70:71]
	v_pk_mul_f32 v[70:71], v[8:9], v[8:9]
	v_pk_add_f32 v[68:69], v[68:69], v[68:69] op_sel:[0,1] op_sel_hi:[1,0]
	v_pk_mov_b32 v[74:75], v[72:73], v[70:71] op_sel:[1,0]
	v_mov_b32_e32 v73, v71
	v_pk_add_f32 v[70:71], v[74:75], v[72:73]
	v_mul_f32_e32 v72, v66, v66
	v_mul_f32_e32 v73, v67, v67
	v_pk_add_f32 v[70:71], v[70:71], v[70:71] op_sel:[0,1] op_sel_hi:[1,0]
	v_pk_fma_f32 v[2:3], v[2:3], s[12:13], v[100:101] op_sel_hi:[1,0,1]
	v_mov_b32_e32 v69, v72
	v_mov_b32_e32 v71, v73
	v_pk_add_f32 v[68:69], v[68:69], v[70:71]
	v_mul_f32_e32 v70, v3, v3
	v_mul_f32_e32 v72, v1, v1
	v_mul_f32_e32 v74, v64, v64
	v_mul_f32_e32 v75, v65, v65
	v_pk_fma_f32 v[70:71], v[2:3], v[2:3], v[70:71] op_sel_hi:[1,1,0]
	v_pk_fma_f32 v[72:73], v[0:1], v[0:1], v[72:73] op_sel_hi:[1,1,0]
	v_mov_b32_e32 v71, v74
	v_mov_b32_e32 v73, v75
	v_pk_add_f32 v[70:71], v[70:71], v[72:73]
	s_lshl_b64 s[16:17], s[16:17], 13
	v_pk_add_f32 v[68:69], v[68:69], v[70:71]
	s_add_u32 s16, s18, s16
	v_add_f32_e32 v68, v68, v69
	ds_bpermute_b32 v69, v209, v68
	s_addc_u32 s17, s19, s17
	v_mov_b64_e32 v[132:133], v[206:207]
	v_mov_b64_e32 v[134:135], v[204:205]
	v_mov_b64_e32 v[136:137], v[202:203]
	s_waitcnt lgkmcnt(0)
; __device__ __forceinline__ void phase_norm1(const Params& p, const Ctx& F, const int l) {
;     ...
;         float ss = 0.f;
; #pragma unroll
;         for (int j = 0; j < 8; ++j) ss += (v[j].x * v[j].x + v[j].y * v[j].y) + (v[j].z * v[j].z + v[j].w * v[j].w);
;         const float rstd = rsqrtf(wave_sum(ss) * (1.f / DM) + EPS);
;         if (fin) {
; #pragma unroll
;             for (int j = 0; j < 8; ++j) __builtin_nontemporal_store(v[j] * rstd * *((const f32x4*)p.g_final + F.lane + 64 * j), (f32x4*)xd + F.lane + 64 * j);
	v_add_f32_e32 v68, v68, v69
	ds_bpermute_b32 v69, v210, v68
	v_mov_b64_e32 v[138:139], v[200:201]
	v_mov_b64_e32 v[140:141], v[198:199]
	v_mov_b64_e32 v[142:143], v[196:197]
	v_mov_b64_e32 v[144:145], v[194:195]
	s_waitcnt lgkmcnt(0)
	v_add_f32_e32 v68, v68, v69
	ds_bpermute_b32 v69, v211, v68
	v_mov_b64_e32 v[146:147], v[192:193]
	v_mov_b32_e32 v148, v217
	v_mov_b32_e32 v149, v218
	v_mov_b32_e32 v154, v219
	s_waitcnt lgkmcnt(0)
	v_add_f32_e32 v68, v68, v69
	ds_bpermute_b32 v69, v212, v68
	v_mov_b32_e32 v155, v220
	v_mov_b32_e32 v150, v221
	v_mov_b32_e32 v151, v222
	v_mov_b32_e32 v156, v223
	s_waitcnt lgkmcnt(0)
	v_add_f32_e32 v68, v68, v69
	ds_bpermute_b32 v69, v213, v68
	v_mov_b32_e32 v157, v224
	v_mov_b32_e32 v152, v225
	v_mov_b32_e32 v153, v226
	v_mov_b32_e32 v160, v227
	s_waitcnt lgkmcnt(0)
	v_add_f32_e32 v68, v68, v69
	ds_bpermute_b32 v69, v214, v68
	v_mov_b32_e32 v161, v228
	v_mov_b32_e32 v158, v229
	v_mov_b32_e32 v159, v230
	v_mov_b32_e32 v164, v231
	s_waitcnt lgkmcnt(0)
	v_add_f32_e32 v68, v68, v69
	v_fmamk_f32 v68, v68, 0x3a000000, v216
	v_mul_f32_e32 v69, 0x4b800000, v68
	v_cmp_gt_f32_e32 vcc, s31, v68
	v_mov_b32_e32 v165, v232
	v_mov_b32_e32 v162, v233
	v_cndmask_b32_e32 v68, v68, v69, vcc
	v_rsq_f32_e32 v68, v68
	v_mov_b32_e32 v163, v235
	v_mov_b32_e32 v168, v236
	v_mov_b32_e32 v169, v237
	v_mul_f32_e32 v69, 0x45800000, v68
	v_cndmask_b32_e32 v72, v68, v69, vcc
	v_pk_mul_f32 v[28:29], v[28:29], v[72:73] op_sel_hi:[1,0]
	v_pk_mul_f32 v[30:31], v[30:31], v[72:73] op_sel_hi:[1,0]
	s_waitcnt vmcnt(0)
	v_pk_mul_f32 v[12:13], v[12:13], v[28:29]
	v_pk_mul_f32 v[14:15], v[14:15], v[30:31]
	global_store_dwordx4 v128, v[12:15], s[16:17] nt
	v_pk_mul_f32 v[26:27], v[26:27], v[72:73] op_sel_hi:[1,0]
	v_pk_mul_f32 v[24:25], v[24:25], v[72:73] op_sel_hi:[1,0]
	v_pk_mul_f32 v[22:23], v[22:23], v[72:73] op_sel_hi:[1,0]
	v_pk_mul_f32 v[20:21], v[20:21], v[72:73] op_sel_hi:[1,0]
	v_pk_mul_f32 v[18:19], v[18:19], v[72:73] op_sel_hi:[1,0]
	v_pk_mul_f32 v[16:17], v[16:17], v[72:73] op_sel_hi:[1,0]
	v_pk_mul_f32 v[8:9], v[8:9], v[72:73] op_sel_hi:[1,0]
	v_pk_mul_f32 v[10:11], v[10:11], v[72:73] op_sel_hi:[1,0]
	v_mov_b64_e32 v[28:29], v[32:33]
	v_mov_b64_e32 v[30:31], v[34:35]
	v_pk_mul_f32 v[34:35], v[64:65], v[72:73] op_sel_hi:[1,0]
	v_pk_mul_f32 v[32:33], v[66:67], v[72:73] op_sel_hi:[1,0]
	v_mov_b32_e32 v166, v238
	v_mov_b32_e32 v167, v239
	v_mov_b32_e32 v172, v240
	v_mov_b32_e32 v173, v241
	v_mov_b32_e32 v170, v242
	v_mov_b32_e32 v171, v243
	v_mov_b32_e32 v176, v244
	v_mov_b32_e32 v177, v245
	v_mov_b32_e32 v174, v246
	v_mov_b32_e32 v175, v247
	v_mov_b32_e32 v178, v248
	v_mov_b32_e32 v179, v234
	v_pk_mul_f32 v[76:77], v[76:77], v[24:25]
	v_pk_mul_f32 v[78:79], v[78:79], v[26:27]
	global_store_dwordx4 v128, v[76:79], s[16:17] offset:1024 nt
	v_mov_b64_e32 v[24:25], v[36:37]
	v_mov_b64_e32 v[26:27], v[38:39]
	v_pk_mul_f32 v[80:81], v[80:81], v[20:21]
	v_pk_mul_f32 v[82:83], v[82:83], v[22:23]
	global_store_dwordx4 v128, v[80:83], s[16:17] offset:2048 nt
	v_mov_b64_e32 v[20:21], v[40:41]
	v_mov_b64_e32 v[22:23], v[42:43]
	v_pk_mul_f32 v[84:85], v[84:85], v[16:17]
	v_pk_mul_f32 v[86:87], v[86:87], v[18:19]
	global_store_dwordx4 v128, v[84:87], s[16:17] offset:3072 nt
	v_lshl_add_u64 v[16:17], s[16:17], 0, v[128:129]
	v_add_co_u32_e32 v74, vcc, s30, v16
	s_nop 1
	v_addc_co_u32_e32 v75, vcc, 0, v17, vcc
	v_pk_mul_f32 v[16:17], v[4:5], v[72:73] op_sel_hi:[1,0]
	v_pk_mul_f32 v[4:5], v[6:7], v[72:73] op_sel_hi:[1,0]
	s_andn2_b64 vcc, exec, s[14:15]
	v_pk_mul_f32 v[4:5], v[88:89], v[4:5]
	v_pk_mul_f32 v[6:7], v[90:91], v[16:17]
	global_store_dwordx4 v[74:75], v[4:7], off nt
	v_mov_b64_e32 v[12:13], v[48:49]
	v_mov_b64_e32 v[16:17], v[44:45]
	v_mov_b64_e32 v[14:15], v[50:51]
	v_mov_b64_e32 v[18:19], v[46:47]
	v_pk_mul_f32 v[4:5], v[92:93], v[10:11]
	v_pk_mul_f32 v[6:7], v[94:95], v[8:9]
	global_store_dwordx4 v[74:75], v[4:7], off offset:1024 nt
	v_pk_mul_f32 v[8:9], v[0:1], v[72:73] op_sel_hi:[1,0]
	v_pk_mul_f32 v[0:1], v[2:3], v[72:73] op_sel_hi:[1,0]
	v_pk_mul_f32 v[2:3], v[8:9], v[110:111]
	v_pk_mul_f32 v[0:1], v[0:1], v[108:109]
	global_store_dwordx4 v[74:75], v[0:3], off offset:2048 nt
	s_nop 1
	v_mov_b64_e32 v[4:5], v[56:57]
	v_mov_b64_e32 v[0:1], v[60:61]
	v_mov_b64_e32 v[8:9], v[52:53]
	v_mov_b64_e32 v[2:3], v[62:63]
	v_mov_b64_e32 v[6:7], v[58:59]
	v_mov_b64_e32 v[10:11], v[54:55]
	v_pk_mul_f32 v[32:33], v[32:33], v[112:113]
	v_pk_mul_f32 v[34:35], v[34:35], v[114:115]
	global_store_dwordx4 v[74:75], v[32:35], off offset:3072 nt
	s_cbranch_vccz .LBB0_1478
